# speedup vs baseline: 1.0218x; 1.0218x over previous
.LBB1_9:
	s_load_dwordx2 s[18:19], s[0:1], 0x20
	v_and_b32_e32 v101, 63, v0
	s_cmp_lg_u32 s4, 0
	v_lshrrev_b32_e32 v0, 2, v1
	s_cselect_b64 s[20:21], -1, 0
	v_and_or_b32 v100, v102, 12, v0
	s_andn2_b64 vcc, exec, s[8:9]
	s_mov_b32 s17, 0
	s_cbranch_vccnz .LBB1_52
	v_or_b32_e32 v114, 0x20c00, v102
	v_or_b32_e32 v3, 0x20d00, v102
	v_or_b32_e32 v0, 0x20c40, v102
	v_or_b32_e32 v1, 0x20c80, v102
	v_or_b32_e32 v2, 0x20cc0, v102
	v_or_b32_e32 v4, 0x20d40, v102
	v_or_b32_e32 v5, 0x20d80, v102
	v_or_b32_e32 v6, 0x20dc0, v102
	ds_read_b32 v36, v114
	ds_read_b32 v40, v0
	ds_read_b32 v44, v1
	ds_read_b32 v48, v2
	ds_read_b32 v52, v3
	ds_read_b32 v56, v4
	ds_read_b32 v60, v5
	ds_read_b32 v64, v6
	v_lshlrev_b32_e32 v3, 2, v104
	v_lshlrev_b32_e32 v0, 8, v104
	v_lshlrev_b32_e32 v2, 1, v112
	v_and_b32_e32 v4, 12, v3
	s_add_i32 s47, s33, 0x8000
	v_and_b32_e32 v0, 0xf00, v0
	v_bitop3_b32 v3, v2, v3, 12 bitop3:0x78
	v_bitop3_b32 v2, v2, v4, 1 bitop3:0x36
	v_mov_b32_e32 v69, 0
	v_lshlrev_b32_e32 v68, 2, v100
	v_or_b32_e32 v1, s47, v0
	v_lshlrev_b32_e32 v5, 4, v3
	v_lshlrev_b32_e32 v4, 4, v2
	v_and_b32_e32 v6, 48, v104
	v_lshl_add_u64 v[108:109], s[10:11], 0, v[68:69]
	v_add_u32_e32 v0, s33, v0
	s_movk_i32 s0, 0x80
	v_mov_b32_e32 v68, v69
	v_mov_b32_e32 v103, v69
	v_add_u32_e32 v119, v0, v5
	v_add_u32_e32 v120, v0, v4
	v_bitop3_b32 v121, v1, s0, v5 bitop3:0x36
	v_bitop3_b32 v122, v1, s0, v4 bitop3:0x36
	v_mov_b32_e32 v70, v69
	v_mov_b32_e32 v71, v69
	v_add_u32_e32 v123, s43, v6
	v_mov_b64_e32 v[32:33], v[68:69]
	v_mov_b64_e32 v[28:29], v[68:69]
	v_mov_b64_e32 v[24:25], v[68:69]
	v_mov_b64_e32 v[20:21], v[68:69]
	v_mov_b64_e32 v[16:17], v[68:69]
	v_mov_b64_e32 v[12:13], v[68:69]
	v_mov_b64_e32 v[8:9], v[68:69]
	v_mov_b64_e32 v[4:5], v[68:69]
	s_waitcnt lgkmcnt(0)
	v_mov_b32_e32 v37, v36
	v_mov_b32_e32 v38, v36
	v_mov_b32_e32 v39, v36
	v_mov_b32_e32 v41, v40
	v_mov_b32_e32 v42, v40
	v_mov_b32_e32 v43, v40
	v_mov_b32_e32 v45, v44
	v_mov_b32_e32 v46, v44
	v_mov_b32_e32 v47, v44
	v_mov_b32_e32 v49, v48
	v_mov_b32_e32 v50, v48
	v_mov_b32_e32 v51, v48
	v_mov_b32_e32 v53, v52
	v_mov_b32_e32 v54, v52
	v_mov_b32_e32 v55, v52
	v_mov_b32_e32 v57, v56
	v_mov_b32_e32 v58, v56
	v_mov_b32_e32 v59, v56
	v_mov_b32_e32 v61, v60
	v_mov_b32_e32 v62, v60
	v_mov_b32_e32 v63, v60
	v_mov_b32_e32 v65, v64
	v_mov_b32_e32 v66, v64
	v_mov_b32_e32 v67, v64
	v_lshl_add_u64 v[2:3], s[14:15], 0, v[102:103]
	v_lshlrev_b32_e32 v115, 4, v101
	v_lshl_add_u64 v[106:107], s[18:19], 0, v[102:103]
	v_lshlrev_b32_e32 v103, 2, v112
	v_or_b32_e32 v116, 4, v112
	v_or_b32_e32 v117, 8, v112
	v_or_b32_e32 v118, 12, v112
	s_add_i32 s48, s33, 0x8400
	s_add_i32 s49, s33, 0x8800
	s_add_i32 s50, s33, 0x8c00
	s_add_i32 s51, s33, 0x9000
	s_add_i32 s52, s33, 0x9400
	s_add_i32 s53, s33, 0x9800
	s_add_i32 s54, s33, 0x9c00
	v_mov_b32_e32 v1, v100
	s_mov_b32 s45, -1
	s_mov_b32 s16, -16
	s_mov_b32 s14, s6
	s_mov_b32 s15, s7
	v_mov_b32_e32 v124, 0x3727c5ac
	s_movk_i32 s55, 0x4000
	s_mov_b32 s56, 0x24924925
	v_add_u32_e32 v125, 0x400, v114
	v_mov_b32_e32 v126, 0x3f80
	v_mov_b64_e32 v[34:35], v[70:71]
	v_mov_b64_e32 v[30:31], v[70:71]
	v_mov_b64_e32 v[26:27], v[70:71]
	v_mov_b64_e32 v[22:23], v[70:71]
	v_mov_b64_e32 v[18:19], v[70:71]
	v_mov_b64_e32 v[14:15], v[70:71]
	v_mov_b64_e32 v[10:11], v[70:71]
	v_mov_b64_e32 v[6:7], v[70:71]
	v_mov_b32_e32 v0, 0
	s_mov_b32 s46, -1
	s_nop 0
	s_branch .LBB1_12
